# cb1_final_norm_gain_preloaded_once_per_wave
# speedup vs baseline: 1.0127x; 1.0127x over previous
; #define OPQ_LANE() int tid_o_ = (wave << 6) | fresh_lane(), gw_o_ = gw0; asm volatile("" : "+v"(tid_o_), "+s"(gw_o_)); const int tid = tid_o_, lane = tid_o_ & 63, gw = gw_o_; (void)tid; (void)lane; (void)gw
; template <int NTK>
; __device__ __forceinline__ void combine_rows(int t0, int tstride, const LAS int* bst, const int* tok_e, const int* tok_pos, const float* tok_w, const bf16_t* Y, const bf16_t* xbi, float* xio, bf16_t* xb, float* part, const float* gfin, bool last, int lane) {
;     ...
;                 const float r = 1.0f / sqrtf(s * (1.0f / DM) + EPS);
; #pragma unroll
;                 for (int j = 0; j < 4; ++j) { const int c = j * 256 + lane * 4; *(f32x4*)(xio + (size_t)t * DM + c) = v[i][j] * r * *(const f32x4*)(gfin + c); }
; __global__ void __launch_bounds__(512, 2) fwd(Args args) {
;     ...
;         if (IN(pb + 10) && PEN(10)) {
;             OPQ_LANE();
;     ...
;                 for (int t = gw; t < T; t += 4 * NGW) combine_rows<4>(t, NGW, bst, tok_e, tok_pos, tok_w, Yb, XB, rep_ ? (float*)(ws + WS_DUMMY) : xs, rep_ ? (bf16_t*)(ws + WS_DUMMY + 64 * MiB) : XB, rep_ ? (float*)(ws + WS_DUMMY + 96 * MiB) : part, args.in[I_NFIN], l == NL - 1, lane);
.LBB0_1630:
	s_mov_b32 s0, -1
	s_waitcnt lgkmcnt(0)
	s_barrier
	s_nop 0
	v_mbcnt_lo_u32_b32 v0, s0, 0
	v_mbcnt_hi_u32_b32 v0, s0, v0
	v_readlane_b32 s0, v251, 14
	v_or_b32_e32 v0, s55, v0
	s_mov_b32 s12, s0
	s_cmpk_gt_i32 s12, 0x3fff
	s_cbranch_scc1 .LBB0_1660
	v_and_b32_e32 v4, 63, v0
	v_readlane_b32 s2, v251, 32
	v_lshlrev_b32_e32 v160, 2, v4
	v_readlane_b32 s3, v251, 33
	v_lshlrev_b32_e32 v10, 4, v4
	v_mov_b32_e32 v11, v161
	v_lshl_add_u64 v[0:1], s[2:3], 0, v[160:161]
	v_readlane_b32 s2, v253, 52
	v_readlane_b32 s3, v253, 53
	v_readlane_b32 s0, v252, 44
	v_readlane_b32 s1, v252, 45
	v_lshl_add_u64 v[2:3], s[2:3], 0, v[10:11]
	v_readlane_b32 s2, v252, 8
	v_lshlrev_b32_e32 v8, 3, v4
	v_mov_b32_e32 v9, v161
	v_readlane_b32 s3, v252, 9
	s_cmp_lg_u32 s0, 3
	v_cmp_gt_u32_e64 s[0:1], 16, v4
	v_cmp_eq_u32_e64 s[4:5], 0, v4
	v_lshl_add_u64 v[4:5], s[2:3], 0, v[8:9]
	v_readlane_b32 s2, v251, 12
	s_cselect_b64 s[14:15], -1, 0
	v_readlane_b32 s3, v251, 13
	s_ashr_i32 s13, s12, 31
	s_lshl_b32 s16, s12, 1
	v_lshl_add_u64 v[6:7], s[2:3], 0, v[10:11]
	s_lshl_b64 s[2:3], s[12:13], 11
	v_or_b32_e32 v8, s2, v8
	v_mov_b32_e32 v9, s3
	s_lshl_b64 s[2:3], s[12:13], 12
	v_readlane_b32 s6, v252, 27
	s_add_u32 s2, s6, s2
	v_readlane_b32 s6, v252, 28
	s_addc_u32 s3, s6, s3
	v_lshl_add_u64 v[10:11], s[2:3], 0, v[10:11]
	s_lshl_b64 s[2:3], s[12:13], 6
	s_add_u32 s2, s2, 0x200000
	s_addc_u32 s3, s3, 0
	v_lshl_add_u64 v[12:13], s[2:3], 0, v[160:161]
	v_lshlrev_b32_e32 v140, 1, v160
	global_load_dwordx4 v[216:219], v[2:3], off
	global_load_dwordx4 v[220:223], v[2:3], off offset:1024
	global_load_dwordx4 v[224:227], v[2:3], off offset:2048
	global_load_dwordx4 v[228:231], v[2:3], off offset:3072
	s_branch .LBB0_1633

; template <int NTK>
; __device__ __forceinline__ void combine_rows(int t0, int tstride, const LAS int* bst, const int* tok_e, const int* tok_pos, const float* tok_w, const bf16_t* Y, const bf16_t* xbi, float* xio, bf16_t* xb, float* part, const float* gfin, bool last, int lane) {
;     ...
;                 const float r = 1.0f / sqrtf(s * (1.0f / DM) + EPS);
; #pragma unroll
;                 for (int j = 0; j < 4; ++j) { const int c = j * 256 + lane * 4; *(f32x4*)(xio + (size_t)t * DM + c) = v[i][j] * r * *(const f32x4*)(gfin + c); }
.LBB0_1637:
	s_andn2_b64 vcc, exec, s[10:11]
	s_cbranch_vccnz .LBB0_1639
	s_nop 1
	v_mov_b64_e32 v[116:117], v[216:217]
	v_mov_b64_e32 v[118:119], v[218:219]
	v_fmamk_f32 v102, v112, 0x3a800000, v212
	s_mov_b32 s2, 0xf800000
	v_cmp_gt_f32_e32 vcc, s2, v102
	v_mul_f32_e32 v103, 0x4f800000, v102
	s_nop 0
	v_cndmask_b32_e32 v102, v102, v103, vcc
	v_sqrt_f32_e32 v103, v102
	s_nop 0
	v_add_u32_e32 v112, -1, v103
	v_fma_f32 v113, -v112, v103, v102
	v_cmp_ge_f32_e64 s[10:11], 0, v113
	v_add_u32_e32 v113, 1, v103
	s_nop 0
	v_cndmask_b32_e64 v112, v103, v112, s[10:11]
	v_fma_f32 v103, -v113, v103, v102
	v_cmp_lt_f32_e64 s[10:11], 0, v103
	s_nop 1
	v_cndmask_b32_e64 v103, v112, v113, s[10:11]
	v_mul_f32_e32 v112, 0x37800000, v103
	v_cndmask_b32_e32 v103, v103, v112, vcc
	v_cmp_class_f32_e32 vcc, v102, v248
	s_nop 1
	v_cndmask_b32_e32 v102, v103, v102, vcc
	v_div_scale_f32 v103, s[2:3], v102, v102, 1.0
	v_rcp_f32_e32 v112, v103
	s_nop 0
	v_fma_f32 v113, -v103, v112, 1.0
	v_fmac_f32_e32 v112, v113, v112
	v_div_scale_f32 v113, vcc, 1.0, v102, 1.0
	v_mul_f32_e32 v114, v113, v112
	v_fma_f32 v115, -v103, v114, v113
	v_fmac_f32_e32 v114, v115, v112
	v_fma_f32 v103, -v103, v114, v113
	v_div_fmas_f32 v103, v103, v112, v114
	v_div_fixup_f32 v102, v103, v102, 1.0
	v_pk_mul_f32 v[112:113], v[138:139], v[102:103] op_sel_hi:[1,0]
	v_pk_mul_f32 v[114:115], v[136:137], v[102:103] op_sel_hi:[1,0]
	v_pk_mul_f32 v[104:105], v[104:105], v[102:103] op_sel_hi:[1,0]
	v_pk_mul_f32 v[108:109], v[108:109], v[102:103] op_sel_hi:[1,0]
	v_pk_mul_f32 v[110:111], v[110:111], v[102:103] op_sel_hi:[1,0]
	v_pk_mul_f32 v[114:115], v[114:115], v[118:119]
	v_pk_mul_f32 v[112:113], v[112:113], v[116:117]
	global_store_dwordx4 v[10:11], v[112:115], off offset:-3072
	s_nop 1
	v_mov_b64_e32 v[112:113], v[220:221]
	v_mov_b64_e32 v[114:115], v[222:223]
	v_pk_mul_f32 v[112:113], v[108:109], v[112:113]
	v_pk_mul_f32 v[114:115], v[104:105], v[114:115]
	global_store_dwordx4 v[10:11], v[112:115], off offset:-2048
	v_pk_mul_f32 v[108:109], v[106:107], v[102:103] op_sel_hi:[1,0]
	s_nop 1
	v_mov_b64_e32 v[104:105], v[224:225]
	v_mov_b64_e32 v[106:107], v[226:227]
	v_pk_mul_f32 v[104:105], v[110:111], v[104:105]
	v_pk_mul_f32 v[106:107], v[108:109], v[106:107]
	global_store_dwordx4 v[10:11], v[104:107], off offset:-1024
	s_nop 1
	v_pk_mul_f32 v[104:105], v[82:83], v[102:103] op_sel_hi:[1,0]
	v_pk_mul_f32 v[102:103], v[84:85], v[102:103] op_sel_hi:[1,0]
	s_nop 1
	v_mov_b64_e32 v[82:83], v[228:229]
	v_mov_b64_e32 v[84:85], v[230:231]
	v_pk_mul_f32 v[82:83], v[102:103], v[82:83]
	v_pk_mul_f32 v[84:85], v[104:105], v[84:85]
	global_store_dwordx4 v[10:11], v[82:85], off

; template <int NTK>
; __device__ __forceinline__ void combine_rows(int t0, int tstride, const LAS int* bst, const int* tok_e, const int* tok_pos, const float* tok_w, const bf16_t* Y, const bf16_t* xbi, float* xio, bf16_t* xb, float* part, const float* gfin, bool last, int lane) {
;     ...
;                 const float r = 1.0f / sqrtf(s * (1.0f / DM) + EPS);
; #pragma unroll
;                 for (int j = 0; j < 4; ++j) { const int c = j * 256 + lane * 4; *(f32x4*)(xio + (size_t)t * DM + c) = v[i][j] * r * *(const f32x4*)(gfin + c); }
.LBB0_1644:
	s_andn2_b64 vcc, exec, s[10:11]
	s_cbranch_vccnz .LBB0_1646
	v_fmamk_f32 v72, v76, 0x3a800000, v212
	s_mov_b32 s2, 0xf800000
	v_cmp_gt_f32_e32 vcc, s2, v72
	v_mul_f32_e32 v73, 0x4f800000, v72
	s_nop 0
	v_cndmask_b32_e32 v72, v72, v73, vcc
	v_sqrt_f32_e32 v73, v72
	s_nop 0
	v_add_u32_e32 v76, -1, v73
	v_fma_f32 v77, -v76, v73, v72
	v_cmp_ge_f32_e64 s[10:11], 0, v77
	v_add_u32_e32 v77, 1, v73
	s_nop 0
	v_cndmask_b32_e64 v76, v73, v76, s[10:11]
	v_fma_f32 v73, -v77, v73, v72
	v_cmp_lt_f32_e64 s[10:11], 0, v73
	s_nop 1
	v_cndmask_b32_e64 v73, v76, v77, s[10:11]
	v_mul_f32_e32 v76, 0x37800000, v73
	v_cndmask_b32_e32 v73, v73, v76, vcc
	v_cmp_class_f32_e32 vcc, v72, v248
	s_lshl_b64 s[10:11], s[26:27], 12
	s_nop 0
	v_cndmask_b32_e32 v72, v73, v72, vcc
	v_div_scale_f32 v73, s[2:3], v72, v72, 1.0
	v_rcp_f32_e32 v76, v73
	s_nop 0
	v_fma_f32 v77, -v73, v76, 1.0
	v_fmac_f32_e32 v76, v77, v76
	v_div_scale_f32 v77, vcc, 1.0, v72, 1.0
	v_mul_f32_e32 v86, v77, v76
	v_fma_f32 v87, -v73, v86, v77
	v_fmac_f32_e32 v86, v87, v76
	v_fma_f32 v73, -v73, v86, v77
	v_div_fmas_f32 v73, v73, v76, v86
	s_nop 1
	v_mov_b64_e32 v[86:87], v[216:217]
	v_mov_b64_e32 v[88:89], v[218:219]
	v_div_fixup_f32 v72, v73, v72, 1.0
	v_pk_mul_f32 v[76:77], v[92:93], v[72:73] op_sel_hi:[1,0]
	v_pk_mul_f32 v[90:91], v[90:91], v[72:73] op_sel_hi:[1,0]
	v_pk_mul_f32 v[80:81], v[80:81], v[72:73] op_sel_hi:[1,0]
	v_pk_mul_f32 v[64:65], v[64:65], v[72:73] op_sel_hi:[1,0]
	v_pk_mul_f32 v[88:89], v[90:91], v[88:89]
	v_pk_mul_f32 v[86:87], v[76:77], v[86:87]
	v_lshl_add_u64 v[90:91], v[6:7], 0, s[10:11]
	global_store_dwordx4 v[90:91], v[86:89], off
	v_pk_mul_f32 v[76:77], v[82:83], v[72:73] op_sel_hi:[1,0]
	s_nop 0
	v_pk_mul_f32 v[86:87], v[84:85], v[72:73] op_sel_hi:[1,0]
	s_nop 1
	v_mov_b64_e32 v[82:83], v[220:221]
	v_mov_b64_e32 v[84:85], v[222:223]
	v_pk_mul_f32 v[82:83], v[86:87], v[82:83]
	v_pk_mul_f32 v[84:85], v[76:77], v[84:85]
	global_store_dwordx4 v[90:91], v[82:85], off offset:1024
	s_nop 1
	v_pk_mul_f32 v[82:83], v[78:79], v[72:73] op_sel_hi:[1,0]
	s_nop 1
	v_mov_b64_e32 v[76:77], v[224:225]
	v_mov_b64_e32 v[78:79], v[226:227]
	v_pk_mul_f32 v[76:77], v[80:81], v[76:77]
	v_pk_mul_f32 v[78:79], v[82:83], v[78:79]
	global_store_dwordx4 v[90:91], v[76:79], off offset:2048
	s_nop 1
	v_pk_mul_f32 v[76:77], v[74:75], v[72:73] op_sel_hi:[1,0]
	s_nop 1
	v_mov_b64_e32 v[72:73], v[228:229]
	v_mov_b64_e32 v[74:75], v[230:231]
	v_pk_mul_f32 v[72:73], v[64:65], v[72:73]
	v_pk_mul_f32 v[74:75], v[76:77], v[74:75]
	global_store_dwordx4 v[90:91], v[72:75], off offset:3072

; template <int NTK>
; __device__ __forceinline__ void combine_rows(int t0, int tstride, const LAS int* bst, const int* tok_e, const int* tok_pos, const float* tok_w, const bf16_t* Y, const bf16_t* xbi, float* xio, bf16_t* xb, float* part, const float* gfin, bool last, int lane) {
;     ...
;                 const float r = 1.0f / sqrtf(s * (1.0f / DM) + EPS);
; #pragma unroll
;                 for (int j = 0; j < 4; ++j) { const int c = j * 256 + lane * 4; *(f32x4*)(xio + (size_t)t * DM + c) = v[i][j] * r * *(const f32x4*)(gfin + c); }
.LBB0_1651:
	s_andn2_b64 vcc, exec, s[10:11]
	s_cbranch_vccnz .LBB0_1653
	v_fmamk_f32 v20, v38, 0x3a800000, v212
	s_mov_b32 s2, 0xf800000
	v_cmp_gt_f32_e32 vcc, s2, v20
	v_mul_f32_e32 v21, 0x4f800000, v20
	s_nop 0
	v_cndmask_b32_e32 v20, v20, v21, vcc
	v_sqrt_f32_e32 v21, v20
	s_nop 0
	v_add_u32_e32 v38, -1, v21
	v_fma_f32 v39, -v38, v21, v20
	v_cmp_ge_f32_e64 s[10:11], 0, v39
	v_add_u32_e32 v39, 1, v21
	s_nop 0
	v_cndmask_b32_e64 v38, v21, v38, s[10:11]
	v_fma_f32 v21, -v39, v21, v20
	v_cmp_lt_f32_e64 s[10:11], 0, v21
	s_nop 1
	v_cndmask_b32_e64 v21, v38, v39, s[10:11]
	v_mul_f32_e32 v38, 0x37800000, v21
	v_cndmask_b32_e32 v21, v21, v38, vcc
	v_cmp_class_f32_e32 vcc, v20, v248
	s_lshl_b64 s[10:11], s[22:23], 12
	s_nop 0
	v_cndmask_b32_e32 v20, v21, v20, vcc
	v_div_scale_f32 v21, s[2:3], v20, v20, 1.0
	v_rcp_f32_e32 v38, v21
	s_nop 0
	v_fma_f32 v39, -v21, v38, 1.0
	v_fmac_f32_e32 v38, v39, v38
	v_div_scale_f32 v39, vcc, 1.0, v20, 1.0
	v_mul_f32_e32 v56, v39, v38
	v_fma_f32 v57, -v21, v56, v39
	v_fmac_f32_e32 v56, v57, v38
	v_fma_f32 v21, -v21, v56, v39
	v_div_fmas_f32 v21, v21, v38, v56
	v_div_fixup_f32 v20, v21, v20, 1.0
	v_pk_mul_f32 v[38:39], v[54:55], v[20:21] op_sel_hi:[1,0]
	v_pk_mul_f32 v[56:57], v[52:53], v[20:21] op_sel_hi:[1,0]
	s_nop 1
	v_mov_b64_e32 v[52:53], v[216:217]
	v_mov_b64_e32 v[54:55], v[218:219]
	v_pk_mul_f32 v[16:17], v[16:17], v[20:21] op_sel_hi:[1,0]
	v_pk_mul_f32 v[54:55], v[56:57], v[54:55]
	v_pk_mul_f32 v[52:53], v[38:39], v[52:53]
	v_lshl_add_u64 v[56:57], v[6:7], 0, s[10:11]
	global_store_dwordx4 v[56:57], v[52:55], off
	v_pk_mul_f32 v[38:39], v[48:49], v[20:21] op_sel_hi:[1,0]
	s_nop 0
	v_pk_mul_f32 v[52:53], v[50:51], v[20:21] op_sel_hi:[1,0]
	s_nop 1
	v_mov_b64_e32 v[48:49], v[220:221]
	v_mov_b64_e32 v[50:51], v[222:223]
	v_pk_mul_f32 v[48:49], v[52:53], v[48:49]
	v_pk_mul_f32 v[50:51], v[38:39], v[50:51]
	global_store_dwordx4 v[56:57], v[48:51], off offset:1024
	v_pk_mul_f32 v[38:39], v[44:45], v[20:21] op_sel_hi:[1,0]
	s_nop 0
	v_pk_mul_f32 v[48:49], v[46:47], v[20:21] op_sel_hi:[1,0]
	s_nop 1
	v_mov_b64_e32 v[44:45], v[224:225]
	v_mov_b64_e32 v[46:47], v[226:227]
	v_pk_mul_f32 v[44:45], v[48:49], v[44:45]
	v_pk_mul_f32 v[46:47], v[38:39], v[46:47]
	global_store_dwordx4 v[56:57], v[44:47], off offset:2048
	s_nop 1
	v_pk_mul_f32 v[44:45], v[36:37], v[20:21] op_sel_hi:[1,0]
	s_nop 1
	v_mov_b64_e32 v[36:37], v[228:229]
	v_mov_b64_e32 v[38:39], v[230:231]
	v_pk_mul_f32 v[36:37], v[16:17], v[36:37]
	v_pk_mul_f32 v[38:39], v[44:45], v[38:39]
	global_store_dwordx4 v[56:57], v[36:39], off offset:3072

; template <int NTK>
; __device__ __forceinline__ void combine_rows(int t0, int tstride, const LAS int* bst, const int* tok_e, const int* tok_pos, const float* tok_w, const bf16_t* Y, const bf16_t* xbi, float* xio, bf16_t* xb, float* part, const float* gfin, bool last, int lane) {
;     ...
;                 const float r = 1.0f / sqrtf(s * (1.0f / DM) + EPS);
; #pragma unroll
;                 for (int j = 0; j < 4; ++j) { const int c = j * 256 + lane * 4; *(f32x4*)(xio + (size_t)t * DM + c) = v[i][j] * r * *(const f32x4*)(gfin + c); }
.LBB0_1658:
	s_andn2_b64 vcc, exec, s[6:7]
	s_cbranch_vccnz .LBB0_1632
	v_fmamk_f32 v18, v28, 0x3a800000, v212
	s_mov_b32 s2, 0xf800000
	v_cmp_gt_f32_e32 vcc, s2, v18
	v_mul_f32_e32 v19, 0x4f800000, v18
	s_nop 0
	v_cndmask_b32_e32 v18, v18, v19, vcc
	v_sqrt_f32_e32 v19, v18
	s_nop 0
	v_add_u32_e32 v28, -1, v19
	v_fma_f32 v29, -v28, v19, v18
	v_cmp_ge_f32_e64 s[6:7], 0, v29
	v_add_u32_e32 v29, 1, v19
	s_nop 0
	v_cndmask_b32_e64 v28, v19, v28, s[6:7]
	v_fma_f32 v19, -v29, v19, v18
	v_cmp_lt_f32_e64 s[6:7], 0, v19
	s_nop 1
	v_cndmask_b32_e64 v19, v28, v29, s[6:7]
	v_mul_f32_e32 v28, 0x37800000, v19
	v_cndmask_b32_e32 v19, v19, v28, vcc
	v_cmp_class_f32_e32 vcc, v18, v248
	s_lshl_b64 s[6:7], s[18:19], 12
	s_nop 0
	v_cndmask_b32_e32 v18, v19, v18, vcc
	v_div_scale_f32 v19, s[2:3], v18, v18, 1.0
	v_rcp_f32_e32 v28, v19
	s_nop 0
	v_fma_f32 v29, -v19, v28, 1.0
	v_fmac_f32_e32 v28, v29, v28
	v_div_scale_f32 v29, vcc, 1.0, v18, 1.0
	v_mul_f32_e32 v34, v29, v28
	v_fma_f32 v35, -v19, v34, v29
	v_fmac_f32_e32 v34, v35, v28
	v_fma_f32 v19, -v19, v34, v29
	v_div_fmas_f32 v19, v19, v28, v34
	v_div_fixup_f32 v18, v19, v18, 1.0
	v_pk_mul_f32 v[34:35], v[30:31], v[18:19] op_sel_hi:[1,0]
	s_nop 1
	v_mov_b64_e32 v[28:29], v[216:217]
	v_mov_b64_e32 v[30:31], v[218:219]
	v_pk_mul_f32 v[32:33], v[32:33], v[18:19] op_sel_hi:[1,0]
	v_pk_mul_f32 v[16:17], v[16:17], v[18:19] op_sel_hi:[1,0]
	v_pk_mul_f32 v[30:31], v[34:35], v[30:31]
	v_pk_mul_f32 v[28:29], v[32:33], v[28:29]
	v_lshl_add_u64 v[32:33], v[6:7], 0, s[6:7]
	global_store_dwordx4 v[32:33], v[28:31], off
	s_nop 1
	v_pk_mul_f32 v[30:31], v[26:27], v[18:19] op_sel_hi:[1,0]
	s_nop 1
	v_mov_b64_e32 v[26:27], v[220:221]
	v_mov_b64_e32 v[28:29], v[222:223]
	v_pk_mul_f32 v[26:27], v[30:31], v[26:27]
	v_pk_mul_f32 v[28:29], v[16:17], v[28:29]
	global_store_dwordx4 v[32:33], v[26:29], off offset:1024
	v_pk_mul_f32 v[16:17], v[20:21], v[18:19] op_sel_hi:[1,0]
	v_pk_mul_f32 v[20:21], v[24:25], v[18:19] op_sel_hi:[1,0]
	s_nop 1
	v_mov_b64_e32 v[24:25], v[224:225]
	v_mov_b64_e32 v[26:27], v[226:227]
	v_pk_mul_f32 v[24:25], v[20:21], v[24:25]
	v_pk_mul_f32 v[26:27], v[16:17], v[26:27]
	global_store_dwordx4 v[32:33], v[24:27], off offset:2048
	v_pk_mul_f32 v[20:21], v[22:23], v[18:19] op_sel_hi:[1,0]
	v_pk_mul_f32 v[18:19], v[14:15], v[18:19] op_sel_hi:[1,0]
	s_nop 1
	v_mov_b64_e32 v[14:15], v[228:229]
	v_mov_b64_e32 v[16:17], v[230:231]
	v_pk_mul_f32 v[14:15], v[18:19], v[14:15]
	v_pk_mul_f32 v[16:17], v[20:21], v[16:17]
	global_store_dwordx4 v[32:33], v[14:17], off offset:3072
	s_branch .LBB0_1632
